# v9 + P2 per-XCD K-stagger (all WGs of XCD x start at K-tile 4x, wrapping; summation order rotated)
# speedup vs baseline: 1.0008x; 1.0008x over previous
;     __device__ bool next(int i, Unit& u) const { if (!StaticOrder::next(i >> 1, u)) return false; u.kh = i & 1; return true; }
;     __device__ bool next(int i, Unit& u) const { if (i >= 2) return false; u.pm = 0; u.pn = 0; u.e = 0; u.kh = 0; return true; }
;     __device__ bool next(int i, Unit& u) const { if (!StaticOrder::next(i, u)) return false; u.e = tile_e[u.pm]; return true; }
; #define PG8_STAGE(bufoff, gbase, voff) do { _Pragma("unroll") for (int _i = 0; _i < 2; ++_i) \
;         __builtin_amdgcn_global_load_lds((const unsigned*)((const char*)(gbase) + (voff)[_i]), (PG8_LAS unsigned*)(lds + (bufoff) + ldsw + _i * 8192), 16, 0, 0); } while (0)
; #define PG8_WAIT_V(n) asm volatile("s_waitcnt vmcnt(" #n ")" ::: "memory")
; #define PG8_BAR __builtin_amdgcn_s_barrier()
;     __host__ __device__ bool next(int i, Unit& u) const {
;         const long L = (long)i * G + c; if (L >= nwg) return false;
;         int wgid = (int)L; { const int q = nwg / NXCD, r = nwg % NXCD, xcd = wgid % NXCD, off = wgid / NXCD; wgid = (xcd < r ? xcd * (q + 1) : r * (q + 1) + (xcd - r) * q) + off; }
;         const int nig = WGM * nN, gid = wgid / nig, fm = gid * WGM, gsz = (nM - fm) < WGM ? (nM - fm) : WGM;
;         u.pm = fm + ((wgid % nig) % gsz); u.pn = (wgid % nig) / gsz; u.e = 0; u.kh = 0; return true;
; template <class Epi, class Sched, bool ALIGN_EPI = false, bool SP2 = false, bool GATHER = false, bool F8 = false>
; __device__ __forceinline__ void gemm_phase(PG8_LAS unsigned char* lds, const Gemm g, const Sched& S, const Epi& E) {
;     ...
;     const char* cA = (const char*)((Sched::PAIRS && cur.kh) ? g.A2 : g.A) + (GATHER ? (size_t)0 : (size_t)cur.pm * tstep); const char* cB = (const char*)((Sched::PAIRS && cur.kh) ? g.Bt2 : g.Bt) + (size_t)cur.e * g.bgs + (size_t)cur.pn * tstep;
;     S.a_ready(cur);
;     if constexpr (GATHER) load_gather(cur, gc0, gc1);
;     if constexpr (SP2) {
;         PG8_STAGE(PG8_SB(0, 0), cB, voffB); PG8_STAGE(PG8_SB(0, 1), cB + hstep, voffB); PG8_STAGE_A(PG8_SA(0, 0), cA, 0, false); PG8_STAGE_A(PG8_SA(0, 1), cA, 1, false);
;         if (wr == 1) PG8_BAR;
;         PG8_WAIT_V(2); PG8_BAR;
;         PG8_STAGE(PG8_SB(1, 0), cB + kstep, voffB); PG8_STAGE_A(PG8_SA(1, 0), cA + kstep, 0, false); PG8_STAGE(PG8_SB(1, 1), cB + hstep + kstep, voffB);
;         PG8_WAIT_V(6); PG8_BAR;
.LBB0_290:
	s_add_u32 s34, s50, 0x39000000
	s_addc_u32 s35, s51, 0
	s_cmp_lt_i32 s24, 3
	s_cselect_b64 s[0:1], -1, 0
	s_cmp_gt_i32 s25, 2
	s_cselect_b64 s[2:3], -1, 0
	s_and_b64 s[0:1], s[0:1], s[2:3]
	s_andn2_b64 vcc, exec, s[0:1]
	s_cbranch_vccnz .LBB0_480
	s_cmpk_eq_i32 s93, 0x100
	s_cselect_b64 s[4:5], -1, 0
	s_cmpk_lg_i32 s93, 0x100
	v_readlane_b32 s0, v253, 2
	s_cselect_b64 s[8:9], -1, 0
	s_cmpk_gt_i32 s0, 0xe7
	s_cselect_b64 s[0:1], -1, 0
	s_and_b64 s[0:1], s[0:1], s[4:5]
	v_lshlrev_b32_e32 v154, 4, v0
	s_and_b64 vcc, exec, s[0:1]
	s_cbranch_vccnz .LBB0_308
	v_readlane_b32 s2, v253, 2
	s_cmpk_gt_i32 s2, 0xb7f
	v_readfirstlane_b32 s15, v0
	s_cbranch_scc1 .LBB0_308
	v_and_b32_e32 v1, 32, v0
	s_waitcnt vmcnt(9)
	v_bitop3_b32 v10, v154, v1, 48 bitop3:0x6c
	v_bfe_u32 v11, v0, 2, 4
	v_lshrrev_b32_e32 v2, 1, v10
	v_lshrrev_b32_e32 v1, 1, v0
	v_bfe_u32 v3, v0, 2, 2
	v_lshrrev_b32_e32 v4, 3, v0
	v_lshrrev_b32_e32 v7, 5, v0
	v_and_or_b32 v3, v1, 24, v3
	v_and_or_b32 v5, v4, 48, v11
	v_and_or_b32 v6, v1, 32, v2
	v_and_or_b32 v4, v4, 32, v7
	s_lshr_b32 s12, s15, 6
	v_and_or_b32 v4, v4, 36, v3
	v_lshlrev_b32_e32 v6, 1, v6
	v_or_b32_e32 v12, 0x2000, v154
	s_lshr_b32 s16, s15, 8
	s_lshl_b32 s2, s12, 10
	v_lshl_or_b32 v130, v5, 12, v6
	v_lshl_or_b32 v132, v4, 12, v6
	v_lshrrev_b32_e32 v4, 7, v12
	s_movk_i32 s10, 0x70
	v_lshrrev_b32_e32 v6, 5, v154
	s_add_u32 s3, s50, 0x1200000
	v_and_or_b32 v5, v4, s10, v11
	v_and_or_b32 v2, v6, 32, v2
	v_lshrrev_b32_e32 v6, 9, v154
	s_movk_i32 s10, 0x60
	v_readlane_b32 s13, v253, 2
	s_addc_u32 s20, s51, 0
	v_and_or_b32 v4, v4, s10, v6
	s_movk_i32 s10, 0x64
	s_ashr_i32 s21, s13, 31
	v_and_or_b32 v3, v4, s10, v3
	s_lshr_b32 s10, s21, 29
	s_add_i32 s10, s13, s10
	s_ashr_i32 s11, s10, 3
	s_and_b32 s10, s10, -8
	s_sub_i32 s10, s13, s10
	s_cmp_lt_i32 s10, 0
	s_movk_i32 s22, 0x171
	s_cselect_b32 s13, s22, 0x170
	s_mul_i32 s10, s10, s13
	s_add_i32 s10, s10, s11
	s_mul_hi_i32 s11, s10, 0xb21642c9
	s_add_i32 s11, s11, s10
	s_lshr_b32 s13, s11, 31
	s_ashr_i32 s11, s11, 8
	s_add_i32 s11, s11, s13
	s_lshl_b32 s13, s11, 3
	s_mulk_i32 s11, 0x170
	s_sub_i32 s10, s10, s11
	s_sext_i32_i16 s11, s10
	s_bfe_u32 s11, s11, 0x3001c
	s_add_i32 s11, s10, s11
	s_sext_i32_i16 s14, s11
	s_and_b32 s11, s11, 0xfff8
	s_sub_i32 s10, s10, s11
	s_sext_i32_i16 s10, s10
	s_lshr_b32 s14, s14, 3
	v_readlane_b32 s100, v253, 2
	s_and_b32 s100, s100, 7
	s_mul_i32 s100, s100, 6
	s_add_i32 s14, s14, s100
	s_cmp_ge_i32 s14, 46
	s_cselect_b32 s101, 46, 0
	s_sub_i32 s14, s14, s101
	s_add_i32 s58, s13, s10
	s_ashr_i32 s59, s58, 31
	v_readlane_b32 s98, v253, 2
	s_and_b32 s98, s98, 7
	s_lshl_b32 s99, s98, 9
	s_lshl_b32 s98, s98, 2
	s_sub_i32 s98, 28, s98
	s_bfe_i64 s[18:19], s[14:15], 0x100000
	s_lshl_b64 s[10:11], s[58:59], 20
	s_lshl_b64 s[18:19], s[18:19], 20
	s_add_u32 s64, s3, s18
	s_addc_u32 s65, s20, s19
	s_add_u32 s64, s64, s99
	s_addc_u32 s65, s65, 0
	s_add_i32 s23, s2, 0
	s_add_i32 m0, s23, 0x10000
	v_lshlrev_b32_e32 v2, 1, v2
	global_load_lds_dwordx4 v132, s[64:65]
	s_add_i32 m0, s23, 0x12000
	v_lshl_or_b32 v136, v3, 12, v2
	s_add_u32 s18, s64, 0x80000
	global_load_lds_dwordx4 v136, s[64:65]
	s_addc_u32 s19, s65, 0
	s_add_i32 m0, s23, 0x14000
	v_lshl_or_b32 v134, v5, 12, v2
	global_load_lds_dwordx4 v132, s[18:19]
	s_add_i32 m0, s23, 0x16000
	s_add_u32 s60, s6, s10
	s_addc_u32 s61, s7, s11
	s_add_u32 s60, s60, s99
	s_addc_u32 s61, s61, 0
	s_add_i32 s24, s23, 0x2000
	global_load_lds_dwordx4 v136, s[18:19]
	s_mov_b32 m0, s23
	s_add_u32 s10, s60, 0x80000
	global_load_lds_dwordx4 v130, s[60:61]
	s_mov_b32 m0, s24
	s_addc_u32 s11, s61, 0
	s_add_i32 s25, s23, 0x4000
	global_load_lds_dwordx4 v134, s[60:61]
	s_mov_b32 m0, s25
	s_add_i32 s26, s23, 0x6000
	global_load_lds_dwordx4 v130, s[10:11]
	s_mov_b32 m0, s26
	v_mov_b32_e32 v133, 0
	global_load_lds_dwordx4 v134, s[10:11]
	v_mov_b32_e32 v137, v133
	v_mov_b32_e32 v131, v133
	v_mov_b32_e32 v135, v133
	s_cmp_eq_u32 s16, 1
	s_mov_b32 s27, 0
	v_lshl_add_u64 v[8:9], s[64:65], 0, v[132:133]
	v_lshl_add_u64 v[6:7], s[64:65], 0, v[136:137]
	v_lshl_add_u64 v[2:3], s[60:61], 0, v[130:131]
	s_cselect_b64 s[10:11], -1, 0
	s_cmp_lg_u32 s16, 1
	v_lshl_add_u64 v[4:5], s[60:61], 0, v[134:135]
	s_cbranch_scc1 .LBB0_295
	s_barrier

; #define PG8_BAR __builtin_amdgcn_s_barrier()
; template <class Epi, class Sched, bool ALIGN_EPI = false, bool SP2 = false, bool GATHER = false, bool F8 = false>
; __device__ __forceinline__ void gemm_phase(PG8_LAS unsigned char* lds, const Gemm g, const Sched& S, const Epi& E) {
;     ...
;         if (!has_next) break;
;         if (!(Epi::MID && cur.kh == 0)) {
; #pragma unroll
;         for (int a = 0; a < 2; ++a)
; #pragma unroll
;             for (int b = 0; b < 2; ++b)
; #pragma unroll
;                 for (int m = 0; m < 4; ++m)
; #pragma unroll
;                     for (int n = 0; n < 2; ++n) acc[a][b][m][n] = (f32x4){0.f, 0.f, 0.f, 0.f}; }
;         cur = nxt; cA = nA; cB = nB; ++ui;
;         if constexpr (GATHER) { gc0[0] = gn0[0]; gc0[1] = gn0[1]; gc1[0] = gn1[0]; gc1[1] = gn1[1]; }
;         if constexpr (ALIGN_EPI) { if (wr == 1) PG8_BAR; }
.LBB0_297:
	s_andn2_b64 vcc, exec, s[4:5]
	s_mov_b32 s59, s16
	s_mov_b32 s58, s18
	s_mov_b32 s98, s99
	s_mov_b64 s[64:65], s[56:57]
	s_mov_b64 s[60:61], s[54:55]
	s_cbranch_vccz .LBB0_307

;     __device__ bool next(int i, Unit& u) const { if (!StaticOrder::next(i >> 1, u)) return false; u.kh = i & 1; return true; }
;     __device__ bool next(int i, Unit& u) const { if (i >= 2) return false; u.pm = 0; u.pn = 0; u.e = 0; u.kh = 0; return true; }
;     __device__ bool next(int i, Unit& u) const { if (!StaticOrder::next(i, u)) return false; u.e = tile_e[u.pm]; return true; }
; #define PG8_LDA(dst, b, h) do { _Pragma("unroll") for (int m = 0; m < 4; ++m) _Pragma("unroll") for (int k = 0; k < 2; ++k) dst[m][k] = *(const PG8_LAS bf16x8*)(lds + PG8_SA(b, h) + aoff + m * 2048 + k * KFR); } while (0)
; #define PG8_SCHED __builtin_amdgcn_sched_barrier(0)
; template <class Epi, class Sched, bool ALIGN_EPI = false, bool SP2 = false, bool GATHER = false, bool F8 = false>
; __device__ __forceinline__ void gemm_phase(PG8_LAS unsigned char* lds, const Gemm g, const Sched& S, const Epi& E) {
;     ...
;         const bool has_next = S.next(ui + 1, nxt);
;         const char* nA = has_next ? (const char*)((Sched::PAIRS && nxt.kh) ? g.A2 : g.A) + (GATHER ? (size_t)0 : (size_t)nxt.pm * tstep) : cA;
;         if constexpr (GATHER) { if (has_next) load_gather(nxt, gn0, gn1); else { gn0[0] = gc0[0]; gn0[1] = gc0[1]; gn1[0] = gc1[0]; gn1[1] = gc1[1]; } } const char* nB = has_next ? (const char*)((Sched::PAIRS && nxt.kh) ? g.Bt2 : g.Bt) + (size_t)nxt.e * g.bgs + (size_t)nxt.pn * tstep : cB;
;         for (int t = 0; t < nt; t += 2) {
;             const bool last = (t == nt - 2);
;             const char* a1 = cA + (size_t)(t + 1) * kstep;
;             const char* a2 = last ? nA : cA + (size_t)(t + 2) * kstep; const char* b2 = last ? nB : cB + (size_t)(t + 2) * kstep;
;             const char* a3 = a2 + kstep; const char* b3 = b2 + kstep;
;             if (last && has_next) S.a_ready(nxt);
;             if constexpr (SP2) {
;             PG8_LDB(B0, 0, 0); PG8_LDB(B1, 0, 1); PG8_SCHED; PG8_LDA(At, 0, 0); PG8_STAGE_A(PG8_SA(1, 1), a1, 1, false);
;     ...
; #pragma unroll
;         for (int a = 0; a < 2; ++a)
; #pragma unroll
;             for (int b = 0; b < 2; ++b)
; #pragma unroll
;                 for (int m = 0; m < 4; ++m)
; #pragma unroll
;                     for (int n = 0; n < 2; ++n) acc[a][b][m][n] = (f32x4){0.f, 0.f, 0.f, 0.f}; }
.LBB0_300:
	s_add_i32 s16, s16, s100
	s_cmp_ge_i32 s16, 46
	s_cselect_b32 s101, 46, 0
	s_sub_i32 s16, s16, s101
	s_ashr_i32 s19, s18, 31
	s_lshl_b64 s[54:55], s[18:19], 20
	s_add_u32 s54, s6, s54
	s_addc_u32 s55, s7, s55
	v_readlane_b32 vcc_lo, v253, 2
	s_and_b32 vcc_lo, vcc_lo, 7
	s_lshl_b32 vcc_hi, vcc_lo, 2
	s_sub_i32 s99, 28, vcc_hi
	s_lshl_b32 vcc_lo, vcc_lo, 9
	s_add_u32 s54, s54, vcc_lo
	s_addc_u32 s55, s55, 0
	s_and_b64 s[56:57], s[4:5], exec
	s_cselect_b32 s19, s55, s61
	s_cselect_b32 s62, s54, s60
	s_ashr_i32 s17, s16, 31
	s_lshl_b64 s[56:57], s[16:17], 20
	s_add_u32 s56, s3, s56
	s_addc_u32 s57, s20, s57
	s_add_u32 s56, s56, vcc_lo
	s_addc_u32 s57, s57, 0
	s_and_b64 s[66:67], s[4:5], exec
	s_cselect_b32 s17, s57, s65
	s_cselect_b32 s63, s56, s64
	s_add_u32 s66, s64, 0x100
	v_mov_b32_e32 v2, 0
	s_addc_u32 s67, s65, 0
	s_mov_b32 s68, -2
	v_mov_b32_e32 v3, v2
	v_mov_b32_e32 v4, v2
	v_mov_b32_e32 v5, v2
	v_mov_b32_e32 v6, v2
	v_mov_b32_e32 v7, v2
	v_mov_b32_e32 v8, v2
	v_mov_b32_e32 v9, v2
	v_mov_b32_e32 v14, v2
	v_mov_b32_e32 v15, v2
	v_mov_b32_e32 v16, v2
	v_mov_b32_e32 v17, v2
	v_mov_b32_e32 v22, v2
	v_mov_b32_e32 v23, v2
	v_mov_b32_e32 v24, v2
	v_mov_b32_e32 v25, v2
	v_mov_b32_e32 v30, v2
	v_mov_b32_e32 v31, v2
	v_mov_b32_e32 v32, v2
	v_mov_b32_e32 v33, v2
	v_mov_b32_e32 v38, v2
	v_mov_b32_e32 v39, v2
	v_mov_b32_e32 v40, v2
	v_mov_b32_e32 v41, v2
	v_mov_b32_e32 v46, v2
	v_mov_b32_e32 v47, v2
	v_mov_b32_e32 v48, v2
	v_mov_b32_e32 v49, v2
	v_mov_b32_e32 v54, v2
	v_mov_b32_e32 v55, v2
	v_mov_b32_e32 v56, v2
	v_mov_b32_e32 v57, v2
	v_mov_b32_e32 v10, v2
	v_mov_b32_e32 v11, v2
	v_mov_b32_e32 v12, v2
	v_mov_b32_e32 v13, v2
	v_mov_b32_e32 v18, v2
	v_mov_b32_e32 v19, v2
	v_mov_b32_e32 v20, v2
	v_mov_b32_e32 v21, v2
	v_mov_b32_e32 v26, v2
	v_mov_b32_e32 v27, v2
	v_mov_b32_e32 v28, v2
	v_mov_b32_e32 v29, v2
	v_mov_b32_e32 v34, v2
	v_mov_b32_e32 v35, v2
	v_mov_b32_e32 v36, v2
	v_mov_b32_e32 v37, v2
	v_mov_b32_e32 v42, v2
	v_mov_b32_e32 v43, v2
	v_mov_b32_e32 v44, v2
	v_mov_b32_e32 v45, v2
	v_mov_b32_e32 v50, v2
	v_mov_b32_e32 v51, v2
	v_mov_b32_e32 v52, v2
	v_mov_b32_e32 v53, v2
	v_mov_b32_e32 v58, v2
	v_mov_b32_e32 v59, v2
	v_mov_b32_e32 v60, v2
	v_mov_b32_e32 v61, v2
	v_mov_b32_e32 v62, v2
	v_mov_b32_e32 v63, v2
	v_mov_b32_e32 v64, v2
	v_mov_b32_e32 v65, v2
	v_mov_b32_e32 v66, v2
	v_mov_b32_e32 v67, v2
	v_mov_b32_e32 v68, v2
	v_mov_b32_e32 v69, v2
	v_mov_b32_e32 v70, v2
	v_mov_b32_e32 v71, v2
	v_mov_b32_e32 v72, v2
	v_mov_b32_e32 v73, v2
	v_mov_b32_e32 v78, v2
	v_mov_b32_e32 v79, v2
	v_mov_b32_e32 v80, v2
	v_mov_b32_e32 v81, v2
	v_mov_b32_e32 v86, v2
	v_mov_b32_e32 v87, v2
	v_mov_b32_e32 v88, v2
	v_mov_b32_e32 v89, v2
	v_mov_b32_e32 v94, v2
	v_mov_b32_e32 v95, v2
	v_mov_b32_e32 v96, v2
	v_mov_b32_e32 v97, v2
	v_mov_b32_e32 v102, v2
	v_mov_b32_e32 v103, v2
	v_mov_b32_e32 v104, v2
	v_mov_b32_e32 v105, v2
	v_mov_b32_e32 v110, v2
	v_mov_b32_e32 v111, v2
	v_mov_b32_e32 v112, v2
	v_mov_b32_e32 v113, v2
	v_mov_b32_e32 v118, v2
	v_mov_b32_e32 v119, v2
	v_mov_b32_e32 v120, v2
	v_mov_b32_e32 v121, v2
	v_mov_b32_e32 v74, v2
	v_mov_b32_e32 v75, v2
	v_mov_b32_e32 v76, v2
	v_mov_b32_e32 v77, v2
	v_mov_b32_e32 v82, v2
	v_mov_b32_e32 v83, v2
	v_mov_b32_e32 v84, v2
	v_mov_b32_e32 v85, v2
	v_mov_b32_e32 v90, v2
	v_mov_b32_e32 v91, v2
	v_mov_b32_e32 v92, v2
	v_mov_b32_e32 v93, v2
	v_mov_b32_e32 v98, v2
	v_mov_b32_e32 v99, v2
	v_mov_b32_e32 v100, v2
	v_mov_b32_e32 v101, v2
	v_mov_b32_e32 v106, v2
	v_mov_b32_e32 v107, v2
	v_mov_b32_e32 v108, v2
	v_mov_b32_e32 v109, v2
	v_mov_b32_e32 v114, v2
	v_mov_b32_e32 v115, v2
	v_mov_b32_e32 v116, v2
	v_mov_b32_e32 v117, v2
	v_mov_b32_e32 v122, v2
	v_mov_b32_e32 v123, v2
	v_mov_b32_e32 v124, v2
	v_mov_b32_e32 v125, v2
	v_mov_b32_e32 v126, v2
	v_mov_b32_e32 v127, v2
	v_mov_b32_e32 v128, v2
	v_mov_b32_e32 v129, v2
.LBB0_301:
	ds_read_b128 v[156:159], v150
	ds_read_b128 v[160:163], v150 offset:1024
	ds_read_b128 v[164:167], v150 offset:2048
	ds_read_b128 v[168:171], v150 offset:3072
	ds_read_b128 v[172:175], v151
	ds_read_b128 v[176:179], v151 offset:1024
	ds_read_b128 v[180:183], v151 offset:2048
	ds_read_b128 v[184:187], v151 offset:3072
	s_add_u32 s64, s60, 0x100
	s_addc_u32 s65, s61, 0
	s_cmp_eq_u32 s68, s98
	s_cselect_b32 vcc_lo, 0x1000, 0
	s_sub_u32 s64, s64, vcc_lo
	s_subb_u32 s65, s65, 0
	s_cmp_eq_u32 s68, 28
	s_cselect_b32 s79, s19, s65
	s_cselect_b32 s78, s62, s64
	s_cselect_b32 s77, s17, s67
	s_cselect_b32 s76, s63, s66
	v_lshl_add_u64 v[146:147], s[60:61], 0, v[138:139]
	s_add_i32 m0, s23, 0xc000
	ds_read_b128 v[188:191], v152
	ds_read_b128 v[192:195], v152 offset:1024
	ds_read_b128 v[196:199], v152 offset:2048
	ds_read_b128 v[200:203], v152 offset:3072
	ds_read_b128 v[204:207], v152 offset:4096
	ds_read_b128 v[208:211], v152 offset:5120
	ds_read_b128 v[212:215], v152 offset:6144
	ds_read_b128 v[216:219], v152 offset:7168
	global_load_lds_dwordx4 v[146:147], off
	v_lshl_add_u64 v[146:147], s[60:61], 0, v[140:141]
	s_add_i32 m0, s23, 0xe000
	s_nop 0
	global_load_lds_dwordx4 v[146:147], off
	s_waitcnt vmcnt(8)
	s_waitcnt lgkmcnt(0)
	s_barrier
; #define PG8_STAGE(bufoff, gbase, voff) do { _Pragma("unroll") for (int _i = 0; _i < 2; ++_i) \
;         __builtin_amdgcn_global_load_lds((const unsigned*)((const char*)(gbase) + (voff)[_i]), (PG8_LAS unsigned*)(lds + (bufoff) + ldsw + _i * 8192), 16, 0, 0); } while (0)
; #define PG8_LDA(dst, b, h) do { _Pragma("unroll") for (int m = 0; m < 4; ++m) _Pragma("unroll") for (int k = 0; k < 2; ++k) dst[m][k] = *(const PG8_LAS bf16x8*)(lds + PG8_SA(b, h) + aoff + m * 2048 + k * KFR); } while (0)
; #define PG8_LDB(dst, b, h) do { _Pragma("unroll") for (int n = 0; n < 2; ++n) _Pragma("unroll") for (int k = 0; k < 2; ++k) dst[n][k] = *(const PG8_LAS bf16x8*)(lds + PG8_SB(b, h) + boff + n * 2048 + k * KFR); } while (0)
; #define PG8_WAIT_V(n) asm volatile("s_waitcnt vmcnt(" #n ")" ::: "memory")
; #define PG8_WAIT_L(n) asm volatile("s_waitcnt lgkmcnt(" #n ")" ::: "memory")
; #define PG8_BAR __builtin_amdgcn_s_barrier()
; #define PG8_SCHED __builtin_amdgcn_sched_barrier(0)
; template <class Epi, class Sched, bool ALIGN_EPI = false, bool SP2 = false, bool GATHER = false, bool F8 = false>
; __device__ __forceinline__ void gemm_phase(PG8_LAS unsigned char* lds, const Gemm g, const Sched& S, const Epi& E) {
;     ...
;             PG8_LDB(B0, 0, 0); PG8_LDB(B1, 0, 1); PG8_SCHED; PG8_LDA(At, 0, 0); PG8_STAGE_A(PG8_SA(1, 1), a1, 1, false);
;             PG8_WAIT_V(8); PG8_WAIT_L(0); PG8_BAR; PG8_MMA(0, 0, At, B0); PG8_MMA(0, 1, At, B1); PG8_BAR; PG8_SCHED;
;             PG8_LDA(At, 0, 1); PG8_STAGE(PG8_SB(0, 0), b2, voffB); PG8_STAGE(PG8_SB(0, 1), b2 + hstep, voffB); PG8_STAGE_A(PG8_SA(0, 0), a2, 0, last);
;             PG8_WAIT_V(8); PG8_WAIT_L(0); PG8_BAR; PG8_MMA(1, 0, At, B0); PG8_MMA(1, 1, At, B1); PG8_BAR; PG8_SCHED;
	s_setprio 1
	s_waitcnt lgkmcnt(0)
	v_mfma_f32_16x16x32_bf16 v[126:129], v[156:159], v[188:191], v[126:129]
	v_mfma_f32_16x16x32_bf16 v[122:125], v[164:167], v[188:191], v[122:125]
	v_mfma_f32_16x16x32_bf16 v[114:117], v[156:159], v[196:199], v[114:117]
	v_mfma_f32_16x16x32_bf16 v[106:109], v[164:167], v[196:199], v[106:109]
	v_mfma_f32_16x16x32_bf16 v[98:101], v[156:159], v[204:207], v[98:101]
	v_mfma_f32_16x16x32_bf16 v[90:93], v[164:167], v[204:207], v[90:93]
	v_mfma_f32_16x16x32_bf16 v[82:85], v[156:159], v[212:215], v[82:85]
	v_mfma_f32_16x16x32_bf16 v[74:77], v[164:167], v[212:215], v[74:77]
	v_mfma_f32_16x16x32_bf16 v[126:129], v[160:163], v[192:195], v[126:129]
	v_mfma_f32_16x16x32_bf16 v[122:125], v[168:171], v[192:195], v[122:125]
	v_mfma_f32_16x16x32_bf16 v[114:117], v[160:163], v[200:203], v[114:117]
	v_mfma_f32_16x16x32_bf16 v[106:109], v[168:171], v[200:203], v[106:109]
	v_mfma_f32_16x16x32_bf16 v[98:101], v[160:163], v[208:211], v[98:101]
	v_mfma_f32_16x16x32_bf16 v[90:93], v[168:171], v[208:211], v[90:93]
	v_mfma_f32_16x16x32_bf16 v[82:85], v[160:163], v[216:219], v[82:85]
	v_mfma_f32_16x16x32_bf16 v[74:77], v[168:171], v[216:219], v[74:77]
	s_setprio 0
	s_setprio 1
	v_mfma_f32_16x16x32_bf16 v[118:121], v[172:175], v[188:191], v[118:121]
	v_mfma_f32_16x16x32_bf16 v[110:113], v[180:183], v[188:191], v[110:113]
	v_mfma_f32_16x16x32_bf16 v[102:105], v[172:175], v[196:199], v[102:105]
	v_mfma_f32_16x16x32_bf16 v[94:97], v[180:183], v[196:199], v[94:97]
	v_mfma_f32_16x16x32_bf16 v[86:89], v[172:175], v[204:207], v[86:89]
	v_mfma_f32_16x16x32_bf16 v[78:81], v[180:183], v[204:207], v[78:81]
	v_mfma_f32_16x16x32_bf16 v[70:73], v[172:175], v[212:215], v[70:73]
	v_mfma_f32_16x16x32_bf16 v[66:69], v[180:183], v[212:215], v[66:69]
	v_mfma_f32_16x16x32_bf16 v[118:121], v[176:179], v[192:195], v[118:121]
	v_mfma_f32_16x16x32_bf16 v[110:113], v[184:187], v[192:195], v[110:113]
	v_mfma_f32_16x16x32_bf16 v[102:105], v[176:179], v[200:203], v[102:105]
	v_mfma_f32_16x16x32_bf16 v[94:97], v[184:187], v[200:203], v[94:97]
	v_mfma_f32_16x16x32_bf16 v[86:89], v[176:179], v[208:211], v[86:89]
	v_mfma_f32_16x16x32_bf16 v[78:81], v[184:187], v[208:211], v[78:81]
	v_mfma_f32_16x16x32_bf16 v[70:73], v[176:179], v[216:219], v[70:73]
	v_mfma_f32_16x16x32_bf16 v[66:69], v[184:187], v[216:219], v[66:69]
	s_setprio 0
	s_barrier
	s_add_i32 s60, s33, s2
	v_lshl_add_u64 v[146:147], s[76:77], 0, v[132:133]
	s_mov_b32 m0, s60
	ds_read_b128 v[188:191], v152 offset:16384
	ds_read_b128 v[192:195], v152 offset:17408
	ds_read_b128 v[196:199], v152 offset:18432
	ds_read_b128 v[200:203], v152 offset:19456
	ds_read_b128 v[204:207], v152 offset:20480
	ds_read_b128 v[208:211], v152 offset:21504
	ds_read_b128 v[212:215], v152 offset:22528
	ds_read_b128 v[216:219], v152 offset:23552
	global_load_lds_dwordx4 v[146:147], off
	s_add_i32 m0, s60, 0x2000
	s_add_u32 s60, s76, 0x80000
	v_lshl_add_u64 v[220:221], s[76:77], 0, v[136:137]
	s_addc_u32 s61, s77, 0
	s_add_i32 s69, s52, s2
	global_load_lds_dwordx4 v[220:221], off
	v_lshl_add_u64 v[222:223], s[60:61], 0, v[132:133]
	s_mov_b32 m0, s69
	v_lshl_add_u64 v[226:227], s[78:79], 0, v[134:135]
	global_load_lds_dwordx4 v[222:223], off
	v_lshl_add_u64 v[222:223], s[60:61], 0, v[136:137]
	s_add_i32 m0, s69, 0x2000
	s_nop 0
	global_load_lds_dwordx4 v[222:223], off
	v_lshl_add_u64 v[222:223], s[78:79], 0, v[130:131]
	s_mov_b32 m0, s23
	s_nop 0
	global_load_lds_dwordx4 v[222:223], off
	s_mov_b32 m0, s24
	s_nop 0
	global_load_lds_dwordx4 v[226:227], off
	s_waitcnt vmcnt(8)
	s_waitcnt lgkmcnt(0)
	s_barrier
	s_setprio 1
	s_waitcnt lgkmcnt(0)
	v_mfma_f32_16x16x32_bf16 v[62:65], v[156:159], v[188:191], v[62:65]
	v_mfma_f32_16x16x32_bf16 v[58:61], v[164:167], v[188:191], v[58:61]
	v_mfma_f32_16x16x32_bf16 v[50:53], v[156:159], v[196:199], v[50:53]
	v_mfma_f32_16x16x32_bf16 v[42:45], v[164:167], v[196:199], v[42:45]
	v_mfma_f32_16x16x32_bf16 v[34:37], v[156:159], v[204:207], v[34:37]
	v_mfma_f32_16x16x32_bf16 v[26:29], v[164:167], v[204:207], v[26:29]
	v_mfma_f32_16x16x32_bf16 v[18:21], v[156:159], v[212:215], v[18:21]
	v_mfma_f32_16x16x32_bf16 v[10:13], v[164:167], v[212:215], v[10:13]
	v_mfma_f32_16x16x32_bf16 v[62:65], v[160:163], v[192:195], v[62:65]
	v_mfma_f32_16x16x32_bf16 v[58:61], v[168:171], v[192:195], v[58:61]
	v_mfma_f32_16x16x32_bf16 v[50:53], v[160:163], v[200:203], v[50:53]
	v_mfma_f32_16x16x32_bf16 v[42:45], v[168:171], v[200:203], v[42:45]
	v_mfma_f32_16x16x32_bf16 v[34:37], v[160:163], v[208:211], v[34:37]
	v_mfma_f32_16x16x32_bf16 v[26:29], v[168:171], v[208:211], v[26:29]
	v_mfma_f32_16x16x32_bf16 v[18:21], v[160:163], v[216:219], v[18:21]
	v_mfma_f32_16x16x32_bf16 v[10:13], v[168:171], v[216:219], v[10:13]
	s_setprio 0
	s_setprio 1
	v_mfma_f32_16x16x32_bf16 v[54:57], v[172:175], v[188:191], v[54:57]
	v_mfma_f32_16x16x32_bf16 v[46:49], v[180:183], v[188:191], v[46:49]
	v_mfma_f32_16x16x32_bf16 v[38:41], v[172:175], v[196:199], v[38:41]
	v_mfma_f32_16x16x32_bf16 v[30:33], v[180:183], v[196:199], v[30:33]
	v_mfma_f32_16x16x32_bf16 v[22:25], v[172:175], v[204:207], v[22:25]
	v_mfma_f32_16x16x32_bf16 v[14:17], v[180:183], v[204:207], v[14:17]
	v_mfma_f32_16x16x32_bf16 v[6:9], v[172:175], v[212:215], v[6:9]
	v_mfma_f32_16x16x32_bf16 v[2:5], v[180:183], v[212:215], v[2:5]
	v_mfma_f32_16x16x32_bf16 v[54:57], v[176:179], v[192:195], v[54:57]
	v_mfma_f32_16x16x32_bf16 v[46:49], v[184:187], v[192:195], v[46:49]
	v_mfma_f32_16x16x32_bf16 v[38:41], v[176:179], v[200:203], v[38:41]
	v_mfma_f32_16x16x32_bf16 v[30:33], v[184:187], v[200:203], v[30:33]
	v_mfma_f32_16x16x32_bf16 v[22:25], v[176:179], v[208:211], v[22:25]
	v_mfma_f32_16x16x32_bf16 v[14:17], v[184:187], v[208:211], v[14:17]
	v_mfma_f32_16x16x32_bf16 v[6:9], v[176:179], v[216:219], v[6:9]
	v_mfma_f32_16x16x32_bf16 v[2:5], v[184:187], v[216:219], v[2:5]
	s_setprio 0
	s_barrier
; #define PG8_LDA(dst, b, h) do { _Pragma("unroll") for (int m = 0; m < 4; ++m) _Pragma("unroll") for (int k = 0; k < 2; ++k) dst[m][k] = *(const PG8_LAS bf16x8*)(lds + PG8_SA(b, h) + aoff + m * 2048 + k * KFR); } while (0)
; #define PG8_LDB(dst, b, h) do { _Pragma("unroll") for (int n = 0; n < 2; ++n) _Pragma("unroll") for (int k = 0; k < 2; ++k) dst[n][k] = *(const PG8_LAS bf16x8*)(lds + PG8_SB(b, h) + boff + n * 2048 + k * KFR); } while (0)
; #define PG8_WAIT_V(n) asm volatile("s_waitcnt vmcnt(" #n ")" ::: "memory")
; #define PG8_WAIT_L(n) asm volatile("s_waitcnt lgkmcnt(" #n ")" ::: "memory")
; #define PG8_BAR __builtin_amdgcn_s_barrier()
; #define PG8_SCHED __builtin_amdgcn_sched_barrier(0)
; template <class Epi, class Sched, bool ALIGN_EPI = false, bool SP2 = false, bool GATHER = false, bool F8 = false>
; __device__ __forceinline__ void gemm_phase(PG8_LAS unsigned char* lds, const Gemm g, const Sched& S, const Epi& E) {
;     ...
;             PG8_LDB(B0, 1, 0); PG8_LDB(B1, 1, 1); PG8_SCHED; PG8_LDA(At, 1, 0); PG8_STAGE_A(PG8_SA(0, 1), a2, 1, last);
;             PG8_WAIT_V(8); PG8_WAIT_L(0); PG8_BAR; PG8_MMA(0, 0, At, B0); PG8_MMA(0, 1, At, B1); PG8_BAR; PG8_SCHED;
	s_add_i32 s69, 0, 0x18000
	v_add_u32_e32 v153, s69, v148
	s_add_i32 s70, 0, 0x1c000
	ds_read_b128 v[156:159], v153
	ds_read_b128 v[160:163], v153 offset:1024
	ds_read_b128 v[164:167], v153 offset:2048
	ds_read_b128 v[168:171], v153 offset:3072
	v_add_u32_e32 v153, s70, v148
	ds_read_b128 v[172:175], v153
	ds_read_b128 v[176:179], v153 offset:1024
	ds_read_b128 v[180:183], v153 offset:2048
	ds_read_b128 v[184:187], v153 offset:3072
	s_add_u32 s60, s78, 0x80000
	s_addc_u32 s61, s79, 0
	s_mov_b32 m0, s25
	v_lshl_add_u64 v[228:229], s[60:61], 0, v[130:131]
	ds_read_b128 v[188:191], v152 offset:32768
	ds_read_b128 v[192:195], v152 offset:33792
	ds_read_b128 v[196:199], v152 offset:34816
	ds_read_b128 v[200:203], v152 offset:35840
	ds_read_b128 v[204:207], v152 offset:36864
	ds_read_b128 v[208:211], v152 offset:37888
	ds_read_b128 v[212:215], v152 offset:38912
	ds_read_b128 v[216:219], v152 offset:39936
	global_load_lds_dwordx4 v[228:229], off
	v_lshl_add_u64 v[228:229], s[60:61], 0, v[134:135]
	s_mov_b32 m0, s26
	s_nop 0
	global_load_lds_dwordx4 v[228:229], off
	s_waitcnt vmcnt(8)
	s_waitcnt lgkmcnt(0)
	s_barrier
	s_setprio 1
	s_waitcnt lgkmcnt(0)
	v_mfma_f32_16x16x32_bf16 v[126:129], v[156:159], v[188:191], v[126:129]
	v_mfma_f32_16x16x32_bf16 v[122:125], v[164:167], v[188:191], v[122:125]
	v_mfma_f32_16x16x32_bf16 v[114:117], v[156:159], v[196:199], v[114:117]
	v_mfma_f32_16x16x32_bf16 v[106:109], v[164:167], v[196:199], v[106:109]
	v_mfma_f32_16x16x32_bf16 v[98:101], v[156:159], v[204:207], v[98:101]
	v_mfma_f32_16x16x32_bf16 v[90:93], v[164:167], v[204:207], v[90:93]
	v_mfma_f32_16x16x32_bf16 v[82:85], v[156:159], v[212:215], v[82:85]
	v_mfma_f32_16x16x32_bf16 v[74:77], v[164:167], v[212:215], v[74:77]
	v_mfma_f32_16x16x32_bf16 v[126:129], v[160:163], v[192:195], v[126:129]
	v_mfma_f32_16x16x32_bf16 v[122:125], v[168:171], v[192:195], v[122:125]
	v_mfma_f32_16x16x32_bf16 v[114:117], v[160:163], v[200:203], v[114:117]
	v_mfma_f32_16x16x32_bf16 v[106:109], v[168:171], v[200:203], v[106:109]
	v_mfma_f32_16x16x32_bf16 v[98:101], v[160:163], v[208:211], v[98:101]
	v_mfma_f32_16x16x32_bf16 v[90:93], v[168:171], v[208:211], v[90:93]
	v_mfma_f32_16x16x32_bf16 v[82:85], v[160:163], v[216:219], v[82:85]
	v_mfma_f32_16x16x32_bf16 v[74:77], v[168:171], v[216:219], v[74:77]
	s_setprio 0
	s_setprio 1
	v_mfma_f32_16x16x32_bf16 v[118:121], v[172:175], v[188:191], v[118:121]
	v_mfma_f32_16x16x32_bf16 v[110:113], v[180:183], v[188:191], v[110:113]
	v_mfma_f32_16x16x32_bf16 v[102:105], v[172:175], v[196:199], v[102:105]
	v_mfma_f32_16x16x32_bf16 v[94:97], v[180:183], v[196:199], v[94:97]
	v_mfma_f32_16x16x32_bf16 v[86:89], v[172:175], v[204:207], v[86:89]
	v_mfma_f32_16x16x32_bf16 v[78:81], v[180:183], v[204:207], v[78:81]
	v_mfma_f32_16x16x32_bf16 v[70:73], v[172:175], v[212:215], v[70:73]
	v_mfma_f32_16x16x32_bf16 v[66:69], v[180:183], v[212:215], v[66:69]
	v_mfma_f32_16x16x32_bf16 v[118:121], v[176:179], v[192:195], v[118:121]
	v_mfma_f32_16x16x32_bf16 v[110:113], v[184:187], v[192:195], v[110:113]
	v_mfma_f32_16x16x32_bf16 v[102:105], v[176:179], v[200:203], v[102:105]
	v_mfma_f32_16x16x32_bf16 v[94:97], v[184:187], v[200:203], v[94:97]
	v_mfma_f32_16x16x32_bf16 v[86:89], v[176:179], v[208:211], v[86:89]
	v_mfma_f32_16x16x32_bf16 v[78:81], v[184:187], v[208:211], v[78:81]
	v_mfma_f32_16x16x32_bf16 v[70:73], v[176:179], v[216:219], v[70:73]
	v_mfma_f32_16x16x32_bf16 v[66:69], v[184:187], v[216:219], v[66:69]
	s_setprio 0
	s_barrier
; #define PG8_STAGE(bufoff, gbase, voff) do { _Pragma("unroll") for (int _i = 0; _i < 2; ++_i) \
;         __builtin_amdgcn_global_load_lds((const unsigned*)((const char*)(gbase) + (voff)[_i]), (PG8_LAS unsigned*)(lds + (bufoff) + ldsw + _i * 8192), 16, 0, 0); } while (0)
; #define PG8_LDA(dst, b, h) do { _Pragma("unroll") for (int m = 0; m < 4; ++m) _Pragma("unroll") for (int k = 0; k < 2; ++k) dst[m][k] = *(const PG8_LAS bf16x8*)(lds + PG8_SA(b, h) + aoff + m * 2048 + k * KFR); } while (0)
; #define PG8_WAIT_V(n) asm volatile("s_waitcnt vmcnt(" #n ")" ::: "memory")
; #define PG8_WAIT_L(n) asm volatile("s_waitcnt lgkmcnt(" #n ")" ::: "memory")
; #define PG8_BAR __builtin_amdgcn_s_barrier()
; #define PG8_SCHED __builtin_amdgcn_sched_barrier(0)
; template <class Epi, class Sched, bool ALIGN_EPI = false, bool SP2 = false, bool GATHER = false, bool F8 = false>
; __device__ __forceinline__ void gemm_phase(PG8_LAS unsigned char* lds, const Gemm g, const Sched& S, const Epi& E) {
;     ...
;         for (int t = 0; t < nt; t += 2) {
;     ...
;             PG8_LDA(At, 1, 1); PG8_STAGE(PG8_SB(1, 0), b3, voffB); PG8_STAGE(PG8_SB(1, 1), b3 + hstep, voffB); PG8_STAGE_A(PG8_SA(1, 0), a3, 0, last);
;             PG8_WAIT_V(8); PG8_WAIT_L(0); PG8_BAR; PG8_MMA(1, 0, At, B0); PG8_MMA(1, 1, At, B1); PG8_BAR; PG8_SCHED;
	s_add_i32 s60, s69, s2
	v_lshl_add_u64 v[146:147], v[146:147], 0, s[12:13]
	s_mov_b32 m0, s60
	ds_read_b128 v[188:191], v152 offset:49152
	ds_read_b128 v[192:195], v152 offset:50176
	ds_read_b128 v[196:199], v152 offset:51200
	ds_read_b128 v[200:203], v152 offset:52224
	ds_read_b128 v[204:207], v152 offset:53248
	ds_read_b128 v[208:211], v152 offset:54272
	ds_read_b128 v[212:215], v152 offset:55296
	ds_read_b128 v[216:219], v152 offset:56320
	global_load_lds_dwordx4 v[146:147], off
	s_add_i32 m0, s60, 0x2000
	s_add_u32 s60, s76, 0x80080
	v_lshl_add_u64 v[146:147], v[220:221], 0, s[12:13]
	s_addc_u32 s61, s77, 0
	s_add_i32 s69, s70, s2
	global_load_lds_dwordx4 v[146:147], off
	v_lshl_add_u64 v[146:147], s[60:61], 0, v[132:133]
	s_mov_b32 m0, s69
	s_nop 0
	global_load_lds_dwordx4 v[146:147], off
	v_lshl_add_u64 v[146:147], s[60:61], 0, v[136:137]
	s_add_i32 m0, s69, 0x2000
	s_nop 0
	global_load_lds_dwordx4 v[146:147], off
	v_lshl_add_u64 v[146:147], v[222:223], 0, s[12:13]
	s_mov_b32 m0, s30
	s_nop 0
	global_load_lds_dwordx4 v[146:147], off
	v_lshl_add_u64 v[146:147], v[226:227], 0, s[12:13]
	s_mov_b32 m0, s31
	s_nop 0
	global_load_lds_dwordx4 v[146:147], off
	s_waitcnt vmcnt(8)
	s_waitcnt lgkmcnt(0)
	s_barrier
	s_setprio 1
	s_waitcnt lgkmcnt(0)
	v_mfma_f32_16x16x32_bf16 v[62:65], v[156:159], v[188:191], v[62:65]
	v_mfma_f32_16x16x32_bf16 v[58:61], v[164:167], v[188:191], v[58:61]
	v_mfma_f32_16x16x32_bf16 v[50:53], v[156:159], v[196:199], v[50:53]
	v_mfma_f32_16x16x32_bf16 v[42:45], v[164:167], v[196:199], v[42:45]
	v_mfma_f32_16x16x32_bf16 v[34:37], v[156:159], v[204:207], v[34:37]
	v_mfma_f32_16x16x32_bf16 v[26:29], v[164:167], v[204:207], v[26:29]
	v_mfma_f32_16x16x32_bf16 v[18:21], v[156:159], v[212:215], v[18:21]
	v_mfma_f32_16x16x32_bf16 v[10:13], v[164:167], v[212:215], v[10:13]
	v_mfma_f32_16x16x32_bf16 v[62:65], v[160:163], v[192:195], v[62:65]
	v_mfma_f32_16x16x32_bf16 v[58:61], v[168:171], v[192:195], v[58:61]
	v_mfma_f32_16x16x32_bf16 v[50:53], v[160:163], v[200:203], v[50:53]
	v_mfma_f32_16x16x32_bf16 v[42:45], v[168:171], v[200:203], v[42:45]
	v_mfma_f32_16x16x32_bf16 v[34:37], v[160:163], v[208:211], v[34:37]
	v_mfma_f32_16x16x32_bf16 v[26:29], v[168:171], v[208:211], v[26:29]
	v_mfma_f32_16x16x32_bf16 v[18:21], v[160:163], v[216:219], v[18:21]
	v_mfma_f32_16x16x32_bf16 v[10:13], v[168:171], v[216:219], v[10:13]
	s_setprio 0
	s_setprio 1
	v_mfma_f32_16x16x32_bf16 v[54:57], v[172:175], v[188:191], v[54:57]
	v_mfma_f32_16x16x32_bf16 v[46:49], v[180:183], v[188:191], v[46:49]
	v_mfma_f32_16x16x32_bf16 v[38:41], v[172:175], v[196:199], v[38:41]
	v_mfma_f32_16x16x32_bf16 v[30:33], v[180:183], v[196:199], v[30:33]
	v_mfma_f32_16x16x32_bf16 v[22:25], v[172:175], v[204:207], v[22:25]
	v_mfma_f32_16x16x32_bf16 v[14:17], v[180:183], v[204:207], v[14:17]
	v_mfma_f32_16x16x32_bf16 v[6:9], v[172:175], v[212:215], v[6:9]
	v_mfma_f32_16x16x32_bf16 v[2:5], v[180:183], v[212:215], v[2:5]
	v_mfma_f32_16x16x32_bf16 v[54:57], v[176:179], v[192:195], v[54:57]
	v_mfma_f32_16x16x32_bf16 v[46:49], v[184:187], v[192:195], v[46:49]
	v_mfma_f32_16x16x32_bf16 v[38:41], v[176:179], v[200:203], v[38:41]
	v_mfma_f32_16x16x32_bf16 v[30:33], v[184:187], v[200:203], v[30:33]
	v_mfma_f32_16x16x32_bf16 v[22:25], v[176:179], v[208:211], v[22:25]
	v_mfma_f32_16x16x32_bf16 v[14:17], v[184:187], v[208:211], v[14:17]
	v_mfma_f32_16x16x32_bf16 v[6:9], v[176:179], v[216:219], v[6:9]
	v_mfma_f32_16x16x32_bf16 v[2:5], v[184:187], v[216:219], v[2:5]
	s_setprio 0
	s_barrier
	s_add_i32 s68, s68, 2
	s_add_u32 s66, s66, 0x100
	s_addc_u32 s67, s67, 0
	s_cmp_eq_u32 s68, s98
	s_cselect_b32 vcc_lo, 0x1000, 0
	s_sub_u32 s66, s66, vcc_lo
	s_subb_u32 s67, s67, 0
	s_cmp_gt_u32 s68, 29
	s_mov_b64 s[60:61], s[64:65]
	s_cbranch_scc0 .LBB0_301
	s_and_b64 vcc, exec, s[14:15]
	s_cbranch_vccz .LBB0_304
	s_barrier
